# MoE stream loops: next group's weight fragments read quad-by-quad behind the MFMAs; second-half X fragments in own registers, read early
# baseline (speedup 1.0000x reference)
.LBB0_1720:
	s_add_i32 s0, s0, 2
	s_min_u32 s1, s0, 28
	s_lshl_b32 s12, s1, 17
	s_add_i32 s12, s12, 0x60000
	s_add_i32 s58, s85, 0x20000
	s_cmp_gt_u32 s0, 28
	s_cselect_b32 s12, s58, s12
	s_waitcnt vmcnt(12)
	v_cvt_pk_bf16_f32 v164, v74, v78
	s_waitcnt vmcnt(10)
	v_cvt_pk_bf16_f32 v165, v82, v86
	v_cvt_pk_bf16_f32 v166, v75, v79
	v_cvt_pk_bf16_f32 v167, v83, v87
	v_cvt_pk_bf16_f32 v190, v76, v80
	v_cvt_pk_bf16_f32 v191, v84, v88
	v_cvt_pk_bf16_f32 v192, v77, v81
	v_cvt_pk_bf16_f32 v193, v85, v89
	buffer_load_dwordx4 v[74:77], v160, s[8:11], s12 offen nt
	buffer_load_dwordx4 v[78:81], v90, s[8:11], s12 offen nt
	buffer_load_dwordx4 v[82:85], v178, s[8:11], s12 offen nt
	buffer_load_dwordx4 v[86:89], v179, s[8:11], s12 offen nt
	v_add_u32_e32 v194, 0x4000, v188
	v_add_u32_e32 v195, 0x4000, v180
	v_add_u32_e32 v214, v173, v174
	ds_write2_b64 v194, v[164:165], v[166:167] offset1:16
	ds_write2_b64 v195, v[190:191], v[192:193] offset0:32 offset1:48
	v_add_u32_e32 v215, v176, v174
	v_add_u32_e32 v216, v173, v175
	v_add_u32_e32 v217, v176, v175
	ds_read_b128 v[164:167], v214 offset:32768
	ds_read_b128 v[190:193], v214 offset:34816
	ds_read_b128 v[194:197], v214 offset:36864
	ds_read_b128 v[198:201], v215
	ds_read_b128 v[202:205], v215 offset:2048
	ds_read_b128 v[206:209], v215 offset:4096
	ds_read_b128 v[210:213], v215 offset:6144
	ds_read_b128 v[234:237], v216 offset:32768
	ds_read_b128 v[238:241], v216 offset:34816
	ds_read_b128 v[242:245], v216 offset:36864
	s_waitcnt lgkmcnt(6)
	v_mfma_f32_16x16x32_bf16 v[152:155], v[198:201], v[164:167], v[152:155]
	v_mfma_f32_16x16x32_bf16 v[62:65], v[198:201], v[190:193], v[62:65]
	v_mfma_f32_16x16x32_bf16 v[30:33], v[198:201], v[194:197], v[30:33]
	ds_read_b128 v[198:201], v215 offset:8192
	s_waitcnt lgkmcnt(6)
	v_mfma_f32_16x16x32_bf16 v[120:123], v[202:205], v[164:167], v[120:123]
	v_mfma_f32_16x16x32_bf16 v[54:57], v[202:205], v[190:193], v[54:57]
	v_mfma_f32_16x16x32_bf16 v[22:25], v[202:205], v[194:197], v[22:25]
	ds_read_b128 v[202:205], v215 offset:10240
	s_waitcnt lgkmcnt(6)
	v_mfma_f32_16x16x32_bf16 v[112:115], v[206:209], v[164:167], v[112:115]
	v_mfma_f32_16x16x32_bf16 v[46:49], v[206:209], v[190:193], v[46:49]
	v_mfma_f32_16x16x32_bf16 v[14:17], v[206:209], v[194:197], v[14:17]
	ds_read_b128 v[206:209], v215 offset:12288
	s_waitcnt lgkmcnt(6)
	v_mfma_f32_16x16x32_bf16 v[70:73], v[210:213], v[164:167], v[70:73]
	v_mfma_f32_16x16x32_bf16 v[38:41], v[210:213], v[190:193], v[38:41]
	v_mfma_f32_16x16x32_bf16 v[6:9], v[210:213], v[194:197], v[6:9]
	ds_read_b128 v[210:213], v215 offset:14336
	s_waitcnt lgkmcnt(3)
	v_mfma_f32_16x16x32_bf16 v[148:151], v[198:201], v[164:167], v[148:151]
	v_mfma_f32_16x16x32_bf16 v[58:61], v[198:201], v[190:193], v[58:61]
	v_mfma_f32_16x16x32_bf16 v[26:29], v[198:201], v[194:197], v[26:29]
	ds_read_b128 v[198:201], v217
	s_waitcnt lgkmcnt(3)
	v_mfma_f32_16x16x32_bf16 v[116:119], v[202:205], v[164:167], v[116:119]
	v_mfma_f32_16x16x32_bf16 v[50:53], v[202:205], v[190:193], v[50:53]
	v_mfma_f32_16x16x32_bf16 v[18:21], v[202:205], v[194:197], v[18:21]
	ds_read_b128 v[202:205], v217 offset:2048
	s_waitcnt lgkmcnt(3)
	v_mfma_f32_16x16x32_bf16 v[92:95], v[206:209], v[164:167], v[92:95]
	v_mfma_f32_16x16x32_bf16 v[42:45], v[206:209], v[190:193], v[42:45]
	v_mfma_f32_16x16x32_bf16 v[10:13], v[206:209], v[194:197], v[10:13]
	ds_read_b128 v[206:209], v217 offset:4096
	s_waitcnt lgkmcnt(3)
	v_mfma_f32_16x16x32_bf16 v[66:69], v[210:213], v[164:167], v[66:69]
	v_mfma_f32_16x16x32_bf16 v[34:37], v[210:213], v[190:193], v[34:37]
	v_mfma_f32_16x16x32_bf16 v[2:5], v[210:213], v[194:197], v[2:5]
	ds_read_b128 v[210:213], v217 offset:6144
	s_waitcnt lgkmcnt(3)
	v_mfma_f32_16x16x32_bf16 v[152:155], v[198:201], v[234:237], v[152:155]
	v_mfma_f32_16x16x32_bf16 v[62:65], v[198:201], v[238:241], v[62:65]
	v_mfma_f32_16x16x32_bf16 v[30:33], v[198:201], v[242:245], v[30:33]
	ds_read_b128 v[198:201], v217 offset:8192
	s_waitcnt lgkmcnt(3)
	v_mfma_f32_16x16x32_bf16 v[120:123], v[202:205], v[234:237], v[120:123]
	v_mfma_f32_16x16x32_bf16 v[54:57], v[202:205], v[238:241], v[54:57]
	v_mfma_f32_16x16x32_bf16 v[22:25], v[202:205], v[242:245], v[22:25]
	ds_read_b128 v[202:205], v217 offset:10240
	s_waitcnt lgkmcnt(3)
	v_mfma_f32_16x16x32_bf16 v[112:115], v[206:209], v[234:237], v[112:115]
	v_mfma_f32_16x16x32_bf16 v[46:49], v[206:209], v[238:241], v[46:49]
	v_mfma_f32_16x16x32_bf16 v[14:17], v[206:209], v[242:245], v[14:17]
	ds_read_b128 v[206:209], v217 offset:12288
	s_waitcnt lgkmcnt(3)
	v_mfma_f32_16x16x32_bf16 v[70:73], v[210:213], v[234:237], v[70:73]
	v_mfma_f32_16x16x32_bf16 v[38:41], v[210:213], v[238:241], v[38:41]
	v_mfma_f32_16x16x32_bf16 v[6:9], v[210:213], v[242:245], v[6:9]
	ds_read_b128 v[210:213], v217 offset:14336
	s_min_u32 s12, s0, 29
	s_lshl_b32 s12, s12, 7
	s_waitcnt vmcnt(9)
	ds_write_b128 v189, v[132:135] offset:38912
	s_waitcnt vmcnt(8)
	ds_write_b128 v181, v[124:127] offset:39936
	s_waitcnt vmcnt(7)
	ds_write_b128 v189, v[140:143] offset:40960
	s_waitcnt vmcnt(6)
	ds_write_b128 v181, v[144:147] offset:41984
	s_waitcnt vmcnt(5)
	ds_write_b128 v189, v[128:131] offset:43008
	s_waitcnt vmcnt(4)
	ds_write_b128 v181, v[136:139] offset:44032
	s_addk_i32 s12, 0x100
	s_cmp_lt_u32 s0, 30
	s_cbranch_scc1 .Lxk_nx0
	s_cmp_eq_u32 s84, 0
	s_cbranch_scc1 .Lxk_nx0
	s_mov_b32 s12, 0
	v_lshl_or_b32 v182, v246, 12, v163
	v_lshl_or_b32 v183, v247, 12, v163
	v_lshl_or_b32 v184, v248, 12, v163
	v_lshl_or_b32 v185, v249, 12, v163
	v_lshl_or_b32 v186, v250, 12, v163
	v_lshl_or_b32 v187, v251, 12, v163
.Lxk_nx0:
	s_waitcnt lgkmcnt(9)
	v_mfma_f32_16x16x32_bf16 v[148:151], v[198:201], v[234:237], v[148:151]
	buffer_load_dwordx4 v[124:127], v182, s[4:7], s12 offen
	buffer_load_dwordx4 v[128:131], v183, s[4:7], s12 offen
	buffer_load_dwordx4 v[132:135], v184, s[4:7], s12 offen
	buffer_load_dwordx4 v[136:139], v185, s[4:7], s12 offen
	buffer_load_dwordx4 v[140:143], v186, s[4:7], s12 offen
	buffer_load_dwordx4 v[144:147], v187, s[4:7], s12 offen
	s_min_u32 s12, s0, 27
	s_waitcnt lgkmcnt(0)
	v_mfma_f32_16x16x32_bf16 v[116:119], v[202:205], v[234:237], v[116:119]
	s_barrier
	s_lshl_b32 s12, s12, 17
	v_mfma_f32_16x16x32_bf16 v[92:95], v[206:209], v[234:237], v[92:95]
	s_add_i32 s12, s12, 0x80000
	s_sub_i32 s58, s0, 28
	s_lshl_b32 s58, s58, 17
	s_add_i32 s58, s58, s85
	s_cmp_gt_u32 s0, 27
	s_cselect_b32 s12, s58, s12
	v_mfma_f32_16x16x32_bf16 v[66:69], v[210:213], v[234:237], v[66:69]
	v_cvt_pk_bf16_f32 v164, v96, v100
	v_cvt_pk_bf16_f32 v165, v104, v108
	v_cvt_pk_bf16_f32 v96, v97, v101
	v_cvt_pk_bf16_f32 v97, v105, v109
	ds_write2_b64 v188, v[164:165], v[96:97] offset1:16
	v_cvt_pk_bf16_f32 v96, v98, v102
	v_cvt_pk_bf16_f32 v97, v106, v110
	v_cvt_pk_bf16_f32 v98, v99, v103
	v_cvt_pk_bf16_f32 v99, v107, v111
	ds_write2_b64 v180, v[96:97], v[98:99] offset0:32 offset1:48
	buffer_load_dwordx4 v[96:99], v160, s[8:11], s12 offen nt
	buffer_load_dwordx4 v[100:103], v90, s[8:11], s12 offen nt
	buffer_load_dwordx4 v[104:107], v178, s[8:11], s12 offen nt
	buffer_load_dwordx4 v[108:111], v179, s[8:11], s12 offen nt
	v_mfma_f32_16x16x32_bf16 v[58:61], v[198:201], v[238:241], v[58:61]
	v_mfma_f32_16x16x32_bf16 v[26:29], v[198:201], v[242:245], v[26:29]
	v_mfma_f32_16x16x32_bf16 v[50:53], v[202:205], v[238:241], v[50:53]
	v_mfma_f32_16x16x32_bf16 v[18:21], v[202:205], v[242:245], v[18:21]
	v_mfma_f32_16x16x32_bf16 v[42:45], v[206:209], v[238:241], v[42:45]
	v_mfma_f32_16x16x32_bf16 v[10:13], v[206:209], v[242:245], v[10:13]
	v_mfma_f32_16x16x32_bf16 v[34:37], v[210:213], v[238:241], v[34:37]
	v_mfma_f32_16x16x32_bf16 v[2:5], v[210:213], v[242:245], v[2:5]
	ds_read_b128 v[164:167], v214 offset:38912
	ds_read_b128 v[190:193], v214 offset:40960
	ds_read_b128 v[194:197], v214 offset:43008
	ds_read_b128 v[198:201], v215 offset:16384
	ds_read_b128 v[202:205], v215 offset:18432
	ds_read_b128 v[206:209], v215 offset:20480
	ds_read_b128 v[210:213], v215 offset:22528
	ds_read_b128 v[234:237], v216 offset:38912
	ds_read_b128 v[238:241], v216 offset:40960
	ds_read_b128 v[242:245], v216 offset:43008
	s_waitcnt lgkmcnt(6)
	v_mfma_f32_16x16x32_bf16 v[152:155], v[198:201], v[164:167], v[152:155]
	v_mfma_f32_16x16x32_bf16 v[62:65], v[198:201], v[190:193], v[62:65]
	v_mfma_f32_16x16x32_bf16 v[30:33], v[198:201], v[194:197], v[30:33]
	ds_read_b128 v[198:201], v215 offset:24576
	s_waitcnt lgkmcnt(6)
	v_mfma_f32_16x16x32_bf16 v[120:123], v[202:205], v[164:167], v[120:123]
	v_mfma_f32_16x16x32_bf16 v[54:57], v[202:205], v[190:193], v[54:57]
	v_mfma_f32_16x16x32_bf16 v[22:25], v[202:205], v[194:197], v[22:25]
	ds_read_b128 v[202:205], v215 offset:26624
	s_waitcnt lgkmcnt(6)
	v_mfma_f32_16x16x32_bf16 v[112:115], v[206:209], v[164:167], v[112:115]
	v_mfma_f32_16x16x32_bf16 v[46:49], v[206:209], v[190:193], v[46:49]
	v_mfma_f32_16x16x32_bf16 v[14:17], v[206:209], v[194:197], v[14:17]
	ds_read_b128 v[206:209], v215 offset:28672
	s_waitcnt lgkmcnt(6)
	v_mfma_f32_16x16x32_bf16 v[70:73], v[210:213], v[164:167], v[70:73]
	v_mfma_f32_16x16x32_bf16 v[38:41], v[210:213], v[190:193], v[38:41]
	v_mfma_f32_16x16x32_bf16 v[6:9], v[210:213], v[194:197], v[6:9]
	ds_read_b128 v[210:213], v215 offset:30720
	s_waitcnt lgkmcnt(3)
	v_mfma_f32_16x16x32_bf16 v[148:151], v[198:201], v[164:167], v[148:151]
	v_mfma_f32_16x16x32_bf16 v[58:61], v[198:201], v[190:193], v[58:61]
	v_mfma_f32_16x16x32_bf16 v[26:29], v[198:201], v[194:197], v[26:29]
	ds_read_b128 v[198:201], v217 offset:16384
	s_waitcnt lgkmcnt(3)
	v_mfma_f32_16x16x32_bf16 v[116:119], v[202:205], v[164:167], v[116:119]
	v_mfma_f32_16x16x32_bf16 v[50:53], v[202:205], v[190:193], v[50:53]
	v_mfma_f32_16x16x32_bf16 v[18:21], v[202:205], v[194:197], v[18:21]
	ds_read_b128 v[202:205], v217 offset:18432
	s_waitcnt lgkmcnt(3)
	v_mfma_f32_16x16x32_bf16 v[92:95], v[206:209], v[164:167], v[92:95]
	v_mfma_f32_16x16x32_bf16 v[42:45], v[206:209], v[190:193], v[42:45]
	v_mfma_f32_16x16x32_bf16 v[10:13], v[206:209], v[194:197], v[10:13]
	ds_read_b128 v[206:209], v217 offset:20480
	s_waitcnt lgkmcnt(3)
	v_mfma_f32_16x16x32_bf16 v[66:69], v[210:213], v[164:167], v[66:69]
	v_mfma_f32_16x16x32_bf16 v[34:37], v[210:213], v[190:193], v[34:37]
	v_mfma_f32_16x16x32_bf16 v[2:5], v[210:213], v[194:197], v[2:5]
	ds_read_b128 v[210:213], v217 offset:22528
	s_waitcnt lgkmcnt(3)
	v_mfma_f32_16x16x32_bf16 v[152:155], v[198:201], v[234:237], v[152:155]
	v_mfma_f32_16x16x32_bf16 v[62:65], v[198:201], v[238:241], v[62:65]
	v_mfma_f32_16x16x32_bf16 v[30:33], v[198:201], v[242:245], v[30:33]
	ds_read_b128 v[198:201], v217 offset:24576
	s_waitcnt lgkmcnt(3)
	v_mfma_f32_16x16x32_bf16 v[120:123], v[202:205], v[234:237], v[120:123]
	v_mfma_f32_16x16x32_bf16 v[54:57], v[202:205], v[238:241], v[54:57]
	v_mfma_f32_16x16x32_bf16 v[22:25], v[202:205], v[242:245], v[22:25]
	ds_read_b128 v[202:205], v217 offset:26624
	s_waitcnt lgkmcnt(3)
	v_mfma_f32_16x16x32_bf16 v[112:115], v[206:209], v[234:237], v[112:115]
	v_mfma_f32_16x16x32_bf16 v[46:49], v[206:209], v[238:241], v[46:49]
	v_mfma_f32_16x16x32_bf16 v[14:17], v[206:209], v[242:245], v[14:17]
	ds_read_b128 v[206:209], v217 offset:28672
	s_waitcnt lgkmcnt(3)
	v_mfma_f32_16x16x32_bf16 v[70:73], v[210:213], v[234:237], v[70:73]
	v_mfma_f32_16x16x32_bf16 v[38:41], v[210:213], v[238:241], v[38:41]
	v_mfma_f32_16x16x32_bf16 v[6:9], v[210:213], v[242:245], v[6:9]
	ds_read_b128 v[210:213], v217 offset:30720
	s_lshl_b32 s1, s1, 7
	s_waitcnt vmcnt(9)
	ds_write_b128 v189, v[124:127] offset:32768
	s_waitcnt vmcnt(8)
	ds_write_b128 v181, v[128:131] offset:33792
	s_waitcnt vmcnt(7)
	ds_write_b128 v189, v[132:135] offset:34816
	s_waitcnt vmcnt(6)
	ds_write_b128 v181, v[136:139] offset:35840
	s_waitcnt vmcnt(5)
	ds_write_b128 v189, v[140:143] offset:36864
	s_waitcnt vmcnt(4)
	ds_write_b128 v181, v[144:147] offset:37888
	s_addk_i32 s1, 0x180
	s_cmp_eq_u32 s0, 30
	s_cselect_b32 s58, s84, 0
	s_cmp_lg_u32 s58, 0
	s_cselect_b32 s1, 0x80, s1
	buffer_load_dwordx4 v[132:135], v182, s[4:7], s1 offen
	buffer_load_dwordx4 v[124:127], v183, s[4:7], s1 offen
	buffer_load_dwordx4 v[140:143], v184, s[4:7], s1 offen
	buffer_load_dwordx4 v[144:147], v185, s[4:7], s1 offen
	buffer_load_dwordx4 v[128:131], v186, s[4:7], s1 offen
	buffer_load_dwordx4 v[136:139], v187, s[4:7], s1 offen
	s_waitcnt lgkmcnt(9)
	v_mfma_f32_16x16x32_bf16 v[148:151], v[198:201], v[234:237], v[148:151]
	s_cmp_gt_u32 s0, 29
	s_waitcnt lgkmcnt(0)
	s_barrier
; #define LAS __attribute__((address_space(3)))
; #define MS_WLOAD(set, t) do { _Pragma("unroll") for (int r_ = 0; r_ < 4; ++r_) wr[set][r_] = __builtin_bit_cast(f32x4, __builtin_amdgcn_raw_buffer_load_b128(wrs, (int)wvo + r_ * LDW * 4, MS_CL(t) * (64 * LDW * 4), 0)); } while (0)
; #define MS_WCOMMIT(set, bufi) do { LAS unsigned char* wb_ = lds + (bufi) * MS_TILE; _Pragma("unroll") for (int i_ = 0; i_ < 4; ++i_) { \
;             u32x2 p_; p_.x = pk2(wr[set][0][i_], wr[set][1][i_]); p_.y = pk2(wr[set][2][i_], wr[set][3][i_]); \
;             *(LAS u32x2*)(wb_ + ((i_ < 2) ? lw0 : lw1) + i_ * 128) = p_; } } while (0)
; #define MS_XSLOAD(t) do { _Pragma("unroll") for (int i_ = 0; i_ < 6; ++i_) xs[i_] = __builtin_bit_cast(bf16x8, __builtin_amdgcn_raw_buffer_load_b128(xrs, (int)xso[i_], MS_CL(t) * 128, 0)); } while (0)
; #define MS_XSWRITE(bufi) do { _Pragma("unroll") for (int i_ = 0; i_ < 6; ++i_) *(LAS bf16x8*)(xw + (bufi) * MS_XBUF + i_ * 1024 + ((i_ & 1) ? (xwo ^ 64) : xwo)) = xs[i_]; } while (0)
; #define MS_STEP(I, J, t) do { MS_WCOMMIT(J, J); MS_WLOAD(J, (t) + 3); MS_COMPUTE(I); MS_XSWRITE(J); MS_XSLOAD((t) + 2); __syncthreads(); } while (0)
;     ...
;             const LAS unsigned char* xr1 = lds + MS_XOFF + wave * MS_XWAVE + tk * 128 + (((4 + q) ^ rd_g) << 4);
;             __syncthreads();
;             MS_XSLOAD(0); MS_WLOAD(0, 0); MS_WLOAD(1, 1);
;             MS_WCOMMIT(0, 0); MS_WLOAD(0, 2);
;             MS_XSWRITE(0); MS_XSLOAD(1);
;             __syncthreads();
; #pragma unroll 1
;             for (int t = 0; t < NT; t += 2) { MS_STEP(0, 1, t); MS_STEP(1, 0, t + 1); }
	v_mfma_f32_16x16x32_bf16 v[58:61], v[198:201], v[238:241], v[58:61]
	v_mfma_f32_16x16x32_bf16 v[26:29], v[198:201], v[242:245], v[26:29]
	v_mfma_f32_16x16x32_bf16 v[116:119], v[202:205], v[234:237], v[116:119]
	v_mfma_f32_16x16x32_bf16 v[50:53], v[202:205], v[238:241], v[50:53]
	v_mfma_f32_16x16x32_bf16 v[18:21], v[202:205], v[242:245], v[18:21]
	v_mfma_f32_16x16x32_bf16 v[92:95], v[206:209], v[234:237], v[92:95]
	v_mfma_f32_16x16x32_bf16 v[42:45], v[206:209], v[238:241], v[42:45]
	v_mfma_f32_16x16x32_bf16 v[10:13], v[206:209], v[242:245], v[10:13]
	v_mfma_f32_16x16x32_bf16 v[66:69], v[210:213], v[234:237], v[66:69]
	v_mfma_f32_16x16x32_bf16 v[34:37], v[210:213], v[238:241], v[34:37]
	v_mfma_f32_16x16x32_bf16 v[2:5], v[210:213], v[242:245], v[2:5]
	s_cbranch_scc0 .LBB0_1720
	s_branch .Lmoe_k_done
.Lmoe_k_b:
	s_add_i32 s0, s0, 2
	s_min_u32 s1, s0, 28
	s_lshl_b32 s12, s1, 17
	s_add_i32 s12, s12, 0x60000
	s_add_i32 s58, s85, 0x20000
	s_cmp_gt_u32 s0, 28
	s_cselect_b32 s12, s58, s12
	s_waitcnt vmcnt(12)
	v_cvt_pk_bf16_f32 v164, v74, v78
	s_waitcnt vmcnt(10)
	v_cvt_pk_bf16_f32 v165, v82, v86
	v_cvt_pk_bf16_f32 v166, v75, v79
	v_cvt_pk_bf16_f32 v167, v83, v87
	v_cvt_pk_bf16_f32 v190, v76, v80
	v_cvt_pk_bf16_f32 v191, v84, v88
	v_cvt_pk_bf16_f32 v192, v77, v81
	v_cvt_pk_bf16_f32 v193, v85, v89
	buffer_load_dwordx4 v[74:77], v160, s[8:11], s12 offen nt
	buffer_load_dwordx4 v[78:81], v90, s[8:11], s12 offen nt
	buffer_load_dwordx4 v[82:85], v178, s[8:11], s12 offen nt
	buffer_load_dwordx4 v[86:89], v179, s[8:11], s12 offen nt
	v_add_u32_e32 v194, 0x4000, v188
	v_add_u32_e32 v195, 0x4000, v180
	v_add_u32_e32 v214, v173, v174
	ds_write2_b64 v194, v[164:165], v[166:167] offset1:16
	ds_write2_b64 v195, v[190:191], v[192:193] offset0:32 offset1:48
	v_add_u32_e32 v215, v176, v174
	v_add_u32_e32 v216, v173, v175
	v_add_u32_e32 v217, v176, v175
	ds_read_b128 v[164:167], v214 offset:32768
	ds_read_b128 v[190:193], v214 offset:34816
	ds_read_b128 v[198:201], v215
	ds_read_b128 v[202:205], v215 offset:2048
	ds_read_b128 v[206:209], v215 offset:4096
	ds_read_b128 v[210:213], v215 offset:6144
	ds_read_b128 v[234:237], v216 offset:32768
	ds_read_b128 v[238:241], v216 offset:34816
	s_waitcnt lgkmcnt(5)
	v_mfma_f32_16x16x32_bf16 v[152:155], v[198:201], v[164:167], v[152:155]
	v_mfma_f32_16x16x32_bf16 v[62:65], v[198:201], v[190:193], v[62:65]
	ds_read_b128 v[198:201], v215 offset:8192
	s_waitcnt lgkmcnt(5)
	v_mfma_f32_16x16x32_bf16 v[120:123], v[202:205], v[164:167], v[120:123]
	v_mfma_f32_16x16x32_bf16 v[54:57], v[202:205], v[190:193], v[54:57]
	ds_read_b128 v[202:205], v215 offset:10240
	s_waitcnt lgkmcnt(5)
	v_mfma_f32_16x16x32_bf16 v[112:115], v[206:209], v[164:167], v[112:115]
	v_mfma_f32_16x16x32_bf16 v[46:49], v[206:209], v[190:193], v[46:49]
	ds_read_b128 v[206:209], v215 offset:12288
	s_waitcnt lgkmcnt(5)
	v_mfma_f32_16x16x32_bf16 v[70:73], v[210:213], v[164:167], v[70:73]
	v_mfma_f32_16x16x32_bf16 v[38:41], v[210:213], v[190:193], v[38:41]
	ds_read_b128 v[210:213], v215 offset:14336
	s_waitcnt lgkmcnt(3)
	v_mfma_f32_16x16x32_bf16 v[148:151], v[198:201], v[164:167], v[148:151]
	v_mfma_f32_16x16x32_bf16 v[58:61], v[198:201], v[190:193], v[58:61]
	ds_read_b128 v[198:201], v217
	s_waitcnt lgkmcnt(3)
	v_mfma_f32_16x16x32_bf16 v[116:119], v[202:205], v[164:167], v[116:119]
	v_mfma_f32_16x16x32_bf16 v[50:53], v[202:205], v[190:193], v[50:53]
	ds_read_b128 v[202:205], v217 offset:2048
	s_waitcnt lgkmcnt(3)
	v_mfma_f32_16x16x32_bf16 v[92:95], v[206:209], v[164:167], v[92:95]
	v_mfma_f32_16x16x32_bf16 v[42:45], v[206:209], v[190:193], v[42:45]
	ds_read_b128 v[206:209], v217 offset:4096
	s_waitcnt lgkmcnt(3)
	v_mfma_f32_16x16x32_bf16 v[66:69], v[210:213], v[164:167], v[66:69]
	v_mfma_f32_16x16x32_bf16 v[34:37], v[210:213], v[190:193], v[34:37]
	ds_read_b128 v[210:213], v217 offset:6144
	s_waitcnt lgkmcnt(3)
	v_mfma_f32_16x16x32_bf16 v[152:155], v[198:201], v[234:237], v[152:155]
	v_mfma_f32_16x16x32_bf16 v[62:65], v[198:201], v[238:241], v[62:65]
	ds_read_b128 v[198:201], v217 offset:8192
	s_waitcnt lgkmcnt(3)
	v_mfma_f32_16x16x32_bf16 v[120:123], v[202:205], v[234:237], v[120:123]
	v_mfma_f32_16x16x32_bf16 v[54:57], v[202:205], v[238:241], v[54:57]
	ds_read_b128 v[202:205], v217 offset:10240
	s_waitcnt lgkmcnt(3)
	v_mfma_f32_16x16x32_bf16 v[112:115], v[206:209], v[234:237], v[112:115]
	v_mfma_f32_16x16x32_bf16 v[46:49], v[206:209], v[238:241], v[46:49]
	ds_read_b128 v[206:209], v217 offset:12288
	s_waitcnt lgkmcnt(3)
	v_mfma_f32_16x16x32_bf16 v[70:73], v[210:213], v[234:237], v[70:73]
	v_mfma_f32_16x16x32_bf16 v[38:41], v[210:213], v[238:241], v[38:41]
	ds_read_b128 v[210:213], v217 offset:14336
	s_min_u32 s12, s0, 29
	s_lshl_b32 s12, s12, 7
	s_waitcnt vmcnt(7)
	ds_write_b128 v189, v[132:135] offset:38912
	s_waitcnt vmcnt(6)
	ds_write_b128 v181, v[124:127] offset:39936
	s_waitcnt vmcnt(5)
	ds_write_b128 v189, v[140:143] offset:40960
	s_waitcnt vmcnt(4)
	ds_write_b128 v181, v[144:147] offset:41984
	s_addk_i32 s12, 0x100
	s_cmp_lt_u32 s0, 30
	s_cbranch_scc1 .Lxk_nx1
	s_cmp_eq_u32 s84, 0
	s_cbranch_scc1 .Lxk_nx1
	s_mov_b32 s12, 0
	v_lshl_or_b32 v182, v246, 12, v163
	v_lshl_or_b32 v183, v247, 12, v163
	v_lshl_or_b32 v184, v248, 12, v163
	v_lshl_or_b32 v185, v249, 12, v163
	v_lshl_or_b32 v186, v250, 12, v163
	v_lshl_or_b32 v187, v251, 12, v163
.Lxk_nx1:
	s_waitcnt lgkmcnt(7)
	v_mfma_f32_16x16x32_bf16 v[148:151], v[198:201], v[234:237], v[148:151]
	buffer_load_dwordx4 v[124:127], v182, s[4:7], s12 offen
	buffer_load_dwordx4 v[128:131], v183, s[4:7], s12 offen
	buffer_load_dwordx4 v[132:135], v184, s[4:7], s12 offen
	buffer_load_dwordx4 v[136:139], v185, s[4:7], s12 offen
	s_min_u32 s12, s0, 27
	s_waitcnt lgkmcnt(0)
	v_mfma_f32_16x16x32_bf16 v[116:119], v[202:205], v[234:237], v[116:119]
	s_barrier
	s_lshl_b32 s12, s12, 17
	v_mfma_f32_16x16x32_bf16 v[92:95], v[206:209], v[234:237], v[92:95]
	s_add_i32 s12, s12, 0x80000
	s_sub_i32 s58, s0, 28
	s_lshl_b32 s58, s58, 17
	s_add_i32 s58, s58, s85
	s_cmp_gt_u32 s0, 27
	s_cselect_b32 s12, s58, s12
	v_mfma_f32_16x16x32_bf16 v[66:69], v[210:213], v[234:237], v[66:69]
	v_cvt_pk_bf16_f32 v164, v96, v100
	v_cvt_pk_bf16_f32 v165, v104, v108
	v_cvt_pk_bf16_f32 v96, v97, v101
	v_cvt_pk_bf16_f32 v97, v105, v109
	ds_write2_b64 v188, v[164:165], v[96:97] offset1:16
	v_cvt_pk_bf16_f32 v96, v98, v102
	v_cvt_pk_bf16_f32 v97, v106, v110
	v_cvt_pk_bf16_f32 v98, v99, v103
	v_cvt_pk_bf16_f32 v99, v107, v111
	ds_write2_b64 v180, v[96:97], v[98:99] offset0:32 offset1:48
	buffer_load_dwordx4 v[96:99], v160, s[8:11], s12 offen nt
	buffer_load_dwordx4 v[100:103], v90, s[8:11], s12 offen nt
	buffer_load_dwordx4 v[104:107], v178, s[8:11], s12 offen nt
	buffer_load_dwordx4 v[108:111], v179, s[8:11], s12 offen nt
	v_mfma_f32_16x16x32_bf16 v[58:61], v[198:201], v[238:241], v[58:61]
	v_mfma_f32_16x16x32_bf16 v[50:53], v[202:205], v[238:241], v[50:53]
	v_mfma_f32_16x16x32_bf16 v[42:45], v[206:209], v[238:241], v[42:45]
	v_mfma_f32_16x16x32_bf16 v[34:37], v[210:213], v[238:241], v[34:37]
	ds_read_b128 v[164:167], v214 offset:38912
	ds_read_b128 v[190:193], v214 offset:40960
	ds_read_b128 v[198:201], v215 offset:16384
	ds_read_b128 v[202:205], v215 offset:18432
	ds_read_b128 v[206:209], v215 offset:20480
	ds_read_b128 v[210:213], v215 offset:22528
	ds_read_b128 v[234:237], v216 offset:38912
	ds_read_b128 v[238:241], v216 offset:40960
	s_waitcnt lgkmcnt(5)
	v_mfma_f32_16x16x32_bf16 v[152:155], v[198:201], v[164:167], v[152:155]
	v_mfma_f32_16x16x32_bf16 v[62:65], v[198:201], v[190:193], v[62:65]
	ds_read_b128 v[198:201], v215 offset:24576
	s_waitcnt lgkmcnt(5)
	v_mfma_f32_16x16x32_bf16 v[120:123], v[202:205], v[164:167], v[120:123]
	v_mfma_f32_16x16x32_bf16 v[54:57], v[202:205], v[190:193], v[54:57]
	ds_read_b128 v[202:205], v215 offset:26624
	s_waitcnt lgkmcnt(5)
	v_mfma_f32_16x16x32_bf16 v[112:115], v[206:209], v[164:167], v[112:115]
	v_mfma_f32_16x16x32_bf16 v[46:49], v[206:209], v[190:193], v[46:49]
	ds_read_b128 v[206:209], v215 offset:28672
	s_waitcnt lgkmcnt(5)
	v_mfma_f32_16x16x32_bf16 v[70:73], v[210:213], v[164:167], v[70:73]
	v_mfma_f32_16x16x32_bf16 v[38:41], v[210:213], v[190:193], v[38:41]
	ds_read_b128 v[210:213], v215 offset:30720
	s_waitcnt lgkmcnt(3)
	v_mfma_f32_16x16x32_bf16 v[148:151], v[198:201], v[164:167], v[148:151]
	v_mfma_f32_16x16x32_bf16 v[58:61], v[198:201], v[190:193], v[58:61]
	ds_read_b128 v[198:201], v217 offset:16384
	s_waitcnt lgkmcnt(3)
	v_mfma_f32_16x16x32_bf16 v[116:119], v[202:205], v[164:167], v[116:119]
	v_mfma_f32_16x16x32_bf16 v[50:53], v[202:205], v[190:193], v[50:53]
	ds_read_b128 v[202:205], v217 offset:18432
	s_waitcnt lgkmcnt(3)
	v_mfma_f32_16x16x32_bf16 v[92:95], v[206:209], v[164:167], v[92:95]
	v_mfma_f32_16x16x32_bf16 v[42:45], v[206:209], v[190:193], v[42:45]
	ds_read_b128 v[206:209], v217 offset:20480
	s_waitcnt lgkmcnt(3)
	v_mfma_f32_16x16x32_bf16 v[66:69], v[210:213], v[164:167], v[66:69]
	v_mfma_f32_16x16x32_bf16 v[34:37], v[210:213], v[190:193], v[34:37]
	ds_read_b128 v[210:213], v217 offset:22528
	s_waitcnt lgkmcnt(3)
	v_mfma_f32_16x16x32_bf16 v[152:155], v[198:201], v[234:237], v[152:155]
	v_mfma_f32_16x16x32_bf16 v[62:65], v[198:201], v[238:241], v[62:65]
	ds_read_b128 v[198:201], v217 offset:24576
	s_waitcnt lgkmcnt(3)
	v_mfma_f32_16x16x32_bf16 v[120:123], v[202:205], v[234:237], v[120:123]
	v_mfma_f32_16x16x32_bf16 v[54:57], v[202:205], v[238:241], v[54:57]
	ds_read_b128 v[202:205], v217 offset:26624
	s_waitcnt lgkmcnt(3)
	v_mfma_f32_16x16x32_bf16 v[112:115], v[206:209], v[234:237], v[112:115]
	v_mfma_f32_16x16x32_bf16 v[46:49], v[206:209], v[238:241], v[46:49]
	ds_read_b128 v[206:209], v217 offset:28672
	s_waitcnt lgkmcnt(3)
	v_mfma_f32_16x16x32_bf16 v[70:73], v[210:213], v[234:237], v[70:73]
	v_mfma_f32_16x16x32_bf16 v[38:41], v[210:213], v[238:241], v[38:41]
	ds_read_b128 v[210:213], v217 offset:30720
	s_lshl_b32 s1, s1, 7
	s_waitcnt vmcnt(7)
	ds_write_b128 v189, v[124:127] offset:32768
	s_waitcnt vmcnt(6)
	ds_write_b128 v181, v[128:131] offset:33792
	s_waitcnt vmcnt(5)
	ds_write_b128 v189, v[132:135] offset:34816
	s_waitcnt vmcnt(4)
	ds_write_b128 v181, v[136:139] offset:35840
	s_addk_i32 s1, 0x180
	s_cmp_eq_u32 s0, 30
	s_cselect_b32 s58, s84, 0
	s_cmp_lg_u32 s58, 0
	s_cselect_b32 s1, 0x80, s1
	buffer_load_dwordx4 v[132:135], v182, s[4:7], s1 offen
	buffer_load_dwordx4 v[124:127], v183, s[4:7], s1 offen
	buffer_load_dwordx4 v[140:143], v184, s[4:7], s1 offen
	buffer_load_dwordx4 v[144:147], v185, s[4:7], s1 offen
	s_waitcnt lgkmcnt(7)
	v_mfma_f32_16x16x32_bf16 v[148:151], v[198:201], v[234:237], v[148:151]
	s_cmp_gt_u32 s0, 29
	s_waitcnt lgkmcnt(0)
	s_barrier
	v_mfma_f32_16x16x32_bf16 v[58:61], v[198:201], v[238:241], v[58:61]
	v_mfma_f32_16x16x32_bf16 v[116:119], v[202:205], v[234:237], v[116:119]
	v_mfma_f32_16x16x32_bf16 v[50:53], v[202:205], v[238:241], v[50:53]
	v_mfma_f32_16x16x32_bf16 v[92:95], v[206:209], v[234:237], v[92:95]
	v_mfma_f32_16x16x32_bf16 v[42:45], v[206:209], v[238:241], v[42:45]
	v_mfma_f32_16x16x32_bf16 v[66:69], v[210:213], v[234:237], v[66:69]
	v_mfma_f32_16x16x32_bf16 v[34:37], v[210:213], v[238:241], v[34:37]
	s_cbranch_scc0 .Lmoe_k_b

.LBB0_1785:
	s_add_i32 s2, s2, 2
	s_min_u32 s3, s2, 4
	s_lshl_b32 s33, s3, 19
	s_add_i32 s33, s33, 0x180000
	s_add_i32 s40, s85, 0x80000
	s_cmp_gt_u32 s2, 4
	s_cselect_b32 s33, s40, s33
	s_waitcnt vmcnt(10)
	v_cvt_pk_bf16_f32 v164, v2, v10
	s_waitcnt vmcnt(7)
	v_cvt_pk_bf16_f32 v165, v6, v14
	v_cvt_pk_bf16_f32 v166, v3, v11
	v_cvt_pk_bf16_f32 v167, v7, v15
	v_cvt_pk_bf16_f32 v190, v4, v12
	v_cvt_pk_bf16_f32 v191, v8, v16
	v_cvt_pk_bf16_f32 v192, v5, v13
	v_cvt_pk_bf16_f32 v193, v9, v17
	buffer_load_dwordx4 v[2:5], v160, s[8:11], s33 offen nt
	buffer_load_dwordx4 v[10:13], v90, s[8:11], s33 offen nt
	buffer_load_dwordx4 v[6:9], v178, s[8:11], s33 offen nt
	buffer_load_dwordx4 v[14:17], v179, s[8:11], s33 offen nt
	v_add_u32_e32 v194, 0x4000, v188
	v_add_u32_e32 v195, 0x4000, v180
	v_add_u32_e32 v214, v173, v174
	ds_write2_b64 v194, v[164:165], v[166:167] offset1:16
	ds_write2_b64 v195, v[190:191], v[192:193] offset0:32 offset1:48
	v_add_u32_e32 v215, v176, v174
	v_add_u32_e32 v216, v173, v175
	v_add_u32_e32 v217, v176, v175
	ds_read_b128 v[164:167], v214 offset:32768
	ds_read_b128 v[190:193], v214 offset:34816
	ds_read_b128 v[194:197], v214 offset:36864
	ds_read_b128 v[198:201], v215
	ds_read_b128 v[202:205], v215 offset:2048
	ds_read_b128 v[206:209], v215 offset:4096
	ds_read_b128 v[210:213], v215 offset:6144
	ds_read_b128 v[234:237], v216 offset:32768
	ds_read_b128 v[238:241], v216 offset:34816
	ds_read_b128 v[242:245], v216 offset:36864
	s_waitcnt lgkmcnt(6)
	v_mfma_f32_16x16x32_bf16 v[152:155], v[198:201], v[164:167], v[152:155]
	v_mfma_f32_16x16x32_bf16 v[120:123], v[198:201], v[190:193], v[120:123]
	v_mfma_f32_16x16x32_bf16 v[62:65], v[198:201], v[194:197], v[62:65]
	ds_read_b128 v[198:201], v215 offset:8192
	s_waitcnt lgkmcnt(6)
	v_mfma_f32_16x16x32_bf16 v[148:151], v[202:205], v[164:167], v[148:151]
	v_mfma_f32_16x16x32_bf16 v[96:99], v[202:205], v[190:193], v[96:99]
	v_mfma_f32_16x16x32_bf16 v[58:61], v[202:205], v[194:197], v[58:61]
	ds_read_b128 v[202:205], v215 offset:10240
	s_waitcnt lgkmcnt(6)
	v_mfma_f32_16x16x32_bf16 v[144:147], v[206:209], v[164:167], v[144:147]
	v_mfma_f32_16x16x32_bf16 v[86:89], v[206:209], v[190:193], v[86:89]
	v_mfma_f32_16x16x32_bf16 v[54:57], v[206:209], v[194:197], v[54:57]
	ds_read_b128 v[206:209], v215 offset:12288
	s_waitcnt lgkmcnt(6)
	v_mfma_f32_16x16x32_bf16 v[140:143], v[210:213], v[164:167], v[140:143]
	v_mfma_f32_16x16x32_bf16 v[82:85], v[210:213], v[190:193], v[82:85]
	v_mfma_f32_16x16x32_bf16 v[50:53], v[210:213], v[194:197], v[50:53]
	ds_read_b128 v[210:213], v215 offset:14336
	s_waitcnt lgkmcnt(3)
	v_mfma_f32_16x16x32_bf16 v[136:139], v[198:201], v[164:167], v[136:139]
	v_mfma_f32_16x16x32_bf16 v[78:81], v[198:201], v[190:193], v[78:81]
	v_mfma_f32_16x16x32_bf16 v[46:49], v[198:201], v[194:197], v[46:49]
	ds_read_b128 v[198:201], v217
	s_waitcnt lgkmcnt(3)
	v_mfma_f32_16x16x32_bf16 v[132:135], v[202:205], v[164:167], v[132:135]
	v_mfma_f32_16x16x32_bf16 v[74:77], v[202:205], v[190:193], v[74:77]
	v_mfma_f32_16x16x32_bf16 v[42:45], v[202:205], v[194:197], v[42:45]
	ds_read_b128 v[202:205], v217 offset:2048
	s_waitcnt lgkmcnt(3)
	v_mfma_f32_16x16x32_bf16 v[128:131], v[206:209], v[164:167], v[128:131]
	v_mfma_f32_16x16x32_bf16 v[70:73], v[206:209], v[190:193], v[70:73]
	v_mfma_f32_16x16x32_bf16 v[38:41], v[206:209], v[194:197], v[38:41]
	ds_read_b128 v[206:209], v217 offset:4096
	s_waitcnt lgkmcnt(3)
	v_mfma_f32_16x16x32_bf16 v[124:127], v[210:213], v[164:167], v[124:127]
	v_mfma_f32_16x16x32_bf16 v[66:69], v[210:213], v[190:193], v[66:69]
	v_mfma_f32_16x16x32_bf16 v[34:37], v[210:213], v[194:197], v[34:37]
	ds_read_b128 v[210:213], v217 offset:6144
	s_waitcnt lgkmcnt(3)
	v_mfma_f32_16x16x32_bf16 v[152:155], v[198:201], v[234:237], v[152:155]
	v_mfma_f32_16x16x32_bf16 v[120:123], v[198:201], v[238:241], v[120:123]
	v_mfma_f32_16x16x32_bf16 v[62:65], v[198:201], v[242:245], v[62:65]
	ds_read_b128 v[198:201], v217 offset:8192
	s_waitcnt lgkmcnt(3)
	v_mfma_f32_16x16x32_bf16 v[148:151], v[202:205], v[234:237], v[148:151]
	v_mfma_f32_16x16x32_bf16 v[96:99], v[202:205], v[238:241], v[96:99]
	v_mfma_f32_16x16x32_bf16 v[58:61], v[202:205], v[242:245], v[58:61]
	ds_read_b128 v[202:205], v217 offset:10240
	s_waitcnt lgkmcnt(3)
	v_mfma_f32_16x16x32_bf16 v[144:147], v[206:209], v[234:237], v[144:147]
	v_mfma_f32_16x16x32_bf16 v[86:89], v[206:209], v[238:241], v[86:89]
	v_mfma_f32_16x16x32_bf16 v[54:57], v[206:209], v[242:245], v[54:57]
	ds_read_b128 v[206:209], v217 offset:12288
	s_waitcnt lgkmcnt(3)
	v_mfma_f32_16x16x32_bf16 v[140:143], v[210:213], v[234:237], v[140:143]
	v_mfma_f32_16x16x32_bf16 v[82:85], v[210:213], v[238:241], v[82:85]
	v_mfma_f32_16x16x32_bf16 v[50:53], v[210:213], v[242:245], v[50:53]
	ds_read_b128 v[210:213], v217 offset:14336
	s_min_u32 s33, s2, 5
	s_lshl_b32 s33, s33, 7
	s_waitcnt vmcnt(9)
	ds_write_b128 v189, v[104:107] offset:38912
	s_waitcnt vmcnt(8)
	ds_write_b128 v181, v[92:95] offset:39936
	s_waitcnt vmcnt(7)
	ds_write_b128 v189, v[112:115] offset:40960
	s_waitcnt vmcnt(6)
	ds_write_b128 v181, v[116:119] offset:41984
	s_waitcnt vmcnt(5)
	ds_write_b128 v189, v[100:103] offset:43008
	s_waitcnt vmcnt(4)
	ds_write_b128 v181, v[108:111] offset:44032
	s_addk_i32 s33, 0x100
	s_cmp_lt_u32 s2, 6
	s_cbranch_scc1 .Lxl_nx0
	s_cmp_eq_u32 s84, 0
	s_cbranch_scc1 .Lxl_nx0
	s_mov_b32 s33, 0
	v_add_u32_e32 v252, s87, v162
	v_min_i32_e32 v253, s86, v252
	v_add_u32_e32 v253, s88, v253
	v_lshl_or_b32 v182, v253, 10, v163
	v_or_b32_e32 v253, 8, v252
	v_min_i32_e32 v253, s86, v253
	v_add_u32_e32 v253, s88, v253
	v_lshl_or_b32 v183, v253, 10, v163
	v_add_u32_e32 v253, 0x80, v252
	v_min_i32_e32 v253, s86, v253
	v_add_u32_e32 v253, s88, v253
	v_lshl_or_b32 v184, v253, 10, v163
	v_add_u32_e32 v253, 0x88, v252
	v_min_i32_e32 v253, s86, v253
	v_add_u32_e32 v253, s88, v253
	v_lshl_or_b32 v185, v253, 10, v163
	v_add_u32_e32 v253, 0x100, v252
	v_min_i32_e32 v253, s86, v253
	v_add_u32_e32 v253, s88, v253
	v_lshl_or_b32 v186, v253, 10, v163
	v_add_u32_e32 v253, 0x108, v252
	v_min_i32_e32 v253, s86, v253
	v_add_u32_e32 v253, s88, v253
	v_lshl_or_b32 v187, v253, 10, v163
.Lxl_nx0:
	s_waitcnt lgkmcnt(9)
	v_mfma_f32_16x16x32_bf16 v[136:139], v[198:201], v[234:237], v[136:139]
	buffer_load_dwordx4 v[92:95], v182, s[4:7], s33 offen
	buffer_load_dwordx4 v[100:103], v183, s[4:7], s33 offen
	buffer_load_dwordx4 v[104:107], v184, s[4:7], s33 offen
	buffer_load_dwordx4 v[108:111], v185, s[4:7], s33 offen
	buffer_load_dwordx4 v[112:115], v186, s[4:7], s33 offen
	buffer_load_dwordx4 v[116:119], v187, s[4:7], s33 offen
	s_min_u32 s33, s2, 3
	s_waitcnt lgkmcnt(0)
	v_mfma_f32_16x16x32_bf16 v[132:135], v[202:205], v[234:237], v[132:135]
	s_barrier
	s_lshl_b32 s33, s33, 19
	v_mfma_f32_16x16x32_bf16 v[128:131], v[206:209], v[234:237], v[128:131]
	s_bitset1_b32 s33, 21
	s_sub_i32 s40, s2, 4
	s_lshl_b32 s40, s40, 19
	s_add_i32 s40, s40, s85
	s_cmp_gt_u32 s2, 3
	s_cselect_b32 s33, s40, s33
	v_mfma_f32_16x16x32_bf16 v[124:127], v[210:213], v[234:237], v[124:127]
	v_cvt_pk_bf16_f32 v164, v18, v22
	v_cvt_pk_bf16_f32 v165, v26, v30
	v_cvt_pk_bf16_f32 v18, v19, v23
	v_cvt_pk_bf16_f32 v19, v27, v31
	ds_write2_b64 v188, v[164:165], v[18:19] offset1:16
	v_cvt_pk_bf16_f32 v18, v20, v24
	v_cvt_pk_bf16_f32 v19, v28, v32
	v_cvt_pk_bf16_f32 v20, v21, v25
	v_cvt_pk_bf16_f32 v21, v29, v33
	ds_write2_b64 v180, v[18:19], v[20:21] offset0:32 offset1:48
	buffer_load_dwordx4 v[18:21], v160, s[8:11], s33 offen nt
	buffer_load_dwordx4 v[22:25], v90, s[8:11], s33 offen nt
	buffer_load_dwordx4 v[26:29], v178, s[8:11], s33 offen nt
	buffer_load_dwordx4 v[30:33], v179, s[8:11], s33 offen nt
	v_mfma_f32_16x16x32_bf16 v[78:81], v[198:201], v[238:241], v[78:81]
	v_mfma_f32_16x16x32_bf16 v[46:49], v[198:201], v[242:245], v[46:49]
	v_mfma_f32_16x16x32_bf16 v[74:77], v[202:205], v[238:241], v[74:77]
	v_mfma_f32_16x16x32_bf16 v[42:45], v[202:205], v[242:245], v[42:45]
	v_mfma_f32_16x16x32_bf16 v[70:73], v[206:209], v[238:241], v[70:73]
	v_mfma_f32_16x16x32_bf16 v[38:41], v[206:209], v[242:245], v[38:41]
	v_mfma_f32_16x16x32_bf16 v[66:69], v[210:213], v[238:241], v[66:69]
	v_mfma_f32_16x16x32_bf16 v[34:37], v[210:213], v[242:245], v[34:37]
	ds_read_b128 v[164:167], v214 offset:38912
	ds_read_b128 v[190:193], v214 offset:40960
	ds_read_b128 v[194:197], v214 offset:43008
	ds_read_b128 v[198:201], v215 offset:16384
	ds_read_b128 v[202:205], v215 offset:18432
	ds_read_b128 v[206:209], v215 offset:20480
	ds_read_b128 v[210:213], v215 offset:22528
	ds_read_b128 v[234:237], v216 offset:38912
	ds_read_b128 v[238:241], v216 offset:40960
	ds_read_b128 v[242:245], v216 offset:43008
	s_waitcnt lgkmcnt(6)
	v_mfma_f32_16x16x32_bf16 v[152:155], v[198:201], v[164:167], v[152:155]
	v_mfma_f32_16x16x32_bf16 v[120:123], v[198:201], v[190:193], v[120:123]
	v_mfma_f32_16x16x32_bf16 v[62:65], v[198:201], v[194:197], v[62:65]
	ds_read_b128 v[198:201], v215 offset:24576
	s_waitcnt lgkmcnt(6)
	v_mfma_f32_16x16x32_bf16 v[148:151], v[202:205], v[164:167], v[148:151]
	v_mfma_f32_16x16x32_bf16 v[96:99], v[202:205], v[190:193], v[96:99]
	v_mfma_f32_16x16x32_bf16 v[58:61], v[202:205], v[194:197], v[58:61]
	ds_read_b128 v[202:205], v215 offset:26624
	s_waitcnt lgkmcnt(6)
	v_mfma_f32_16x16x32_bf16 v[144:147], v[206:209], v[164:167], v[144:147]
	v_mfma_f32_16x16x32_bf16 v[86:89], v[206:209], v[190:193], v[86:89]
	v_mfma_f32_16x16x32_bf16 v[54:57], v[206:209], v[194:197], v[54:57]
	ds_read_b128 v[206:209], v215 offset:28672
	s_waitcnt lgkmcnt(6)
	v_mfma_f32_16x16x32_bf16 v[140:143], v[210:213], v[164:167], v[140:143]
	v_mfma_f32_16x16x32_bf16 v[82:85], v[210:213], v[190:193], v[82:85]
	v_mfma_f32_16x16x32_bf16 v[50:53], v[210:213], v[194:197], v[50:53]
	ds_read_b128 v[210:213], v215 offset:30720
	s_waitcnt lgkmcnt(3)
	v_mfma_f32_16x16x32_bf16 v[136:139], v[198:201], v[164:167], v[136:139]
	v_mfma_f32_16x16x32_bf16 v[78:81], v[198:201], v[190:193], v[78:81]
	v_mfma_f32_16x16x32_bf16 v[46:49], v[198:201], v[194:197], v[46:49]
	ds_read_b128 v[198:201], v217 offset:16384
	s_waitcnt lgkmcnt(3)
	v_mfma_f32_16x16x32_bf16 v[132:135], v[202:205], v[164:167], v[132:135]
	v_mfma_f32_16x16x32_bf16 v[74:77], v[202:205], v[190:193], v[74:77]
	v_mfma_f32_16x16x32_bf16 v[42:45], v[202:205], v[194:197], v[42:45]
	ds_read_b128 v[202:205], v217 offset:18432
	s_waitcnt lgkmcnt(3)
	v_mfma_f32_16x16x32_bf16 v[128:131], v[206:209], v[164:167], v[128:131]
	v_mfma_f32_16x16x32_bf16 v[70:73], v[206:209], v[190:193], v[70:73]
	v_mfma_f32_16x16x32_bf16 v[38:41], v[206:209], v[194:197], v[38:41]
	ds_read_b128 v[206:209], v217 offset:20480
	s_waitcnt lgkmcnt(3)
	v_mfma_f32_16x16x32_bf16 v[124:127], v[210:213], v[164:167], v[124:127]
	v_mfma_f32_16x16x32_bf16 v[66:69], v[210:213], v[190:193], v[66:69]
	v_mfma_f32_16x16x32_bf16 v[34:37], v[210:213], v[194:197], v[34:37]
	ds_read_b128 v[210:213], v217 offset:22528
	s_waitcnt lgkmcnt(3)
	v_mfma_f32_16x16x32_bf16 v[152:155], v[198:201], v[234:237], v[152:155]
	v_mfma_f32_16x16x32_bf16 v[120:123], v[198:201], v[238:241], v[120:123]
	v_mfma_f32_16x16x32_bf16 v[62:65], v[198:201], v[242:245], v[62:65]
	ds_read_b128 v[198:201], v217 offset:24576
	s_waitcnt lgkmcnt(3)
	v_mfma_f32_16x16x32_bf16 v[148:151], v[202:205], v[234:237], v[148:151]
	v_mfma_f32_16x16x32_bf16 v[96:99], v[202:205], v[238:241], v[96:99]
	v_mfma_f32_16x16x32_bf16 v[58:61], v[202:205], v[242:245], v[58:61]
	ds_read_b128 v[202:205], v217 offset:26624
	s_waitcnt lgkmcnt(3)
	v_mfma_f32_16x16x32_bf16 v[144:147], v[206:209], v[234:237], v[144:147]
	v_mfma_f32_16x16x32_bf16 v[86:89], v[206:209], v[238:241], v[86:89]
	v_mfma_f32_16x16x32_bf16 v[54:57], v[206:209], v[242:245], v[54:57]
	ds_read_b128 v[206:209], v217 offset:28672
	s_waitcnt lgkmcnt(3)
	v_mfma_f32_16x16x32_bf16 v[140:143], v[210:213], v[234:237], v[140:143]
	v_mfma_f32_16x16x32_bf16 v[82:85], v[210:213], v[238:241], v[82:85]
	v_mfma_f32_16x16x32_bf16 v[50:53], v[210:213], v[242:245], v[50:53]
	ds_read_b128 v[210:213], v217 offset:30720
	s_lshl_b32 s3, s3, 7
	s_waitcnt vmcnt(9)
	ds_write_b128 v189, v[92:95] offset:32768
	s_waitcnt vmcnt(8)
	ds_write_b128 v181, v[100:103] offset:33792
	s_waitcnt vmcnt(7)
	ds_write_b128 v189, v[104:107] offset:34816
	s_waitcnt vmcnt(6)
	ds_write_b128 v181, v[108:111] offset:35840
	s_waitcnt vmcnt(5)
	ds_write_b128 v189, v[112:115] offset:36864
	s_waitcnt vmcnt(4)
	ds_write_b128 v181, v[116:119] offset:37888
	s_addk_i32 s3, 0x180
	s_cmp_eq_u32 s2, 6
	s_cselect_b32 s40, s84, 0
	s_cmp_lg_u32 s40, 0
	s_cselect_b32 s3, 0x80, s3
	buffer_load_dwordx4 v[104:107], v182, s[4:7], s3 offen
	buffer_load_dwordx4 v[92:95], v183, s[4:7], s3 offen
	buffer_load_dwordx4 v[112:115], v184, s[4:7], s3 offen
	buffer_load_dwordx4 v[116:119], v185, s[4:7], s3 offen
	buffer_load_dwordx4 v[100:103], v186, s[4:7], s3 offen
	buffer_load_dwordx4 v[108:111], v187, s[4:7], s3 offen
	s_waitcnt lgkmcnt(9)
	v_mfma_f32_16x16x32_bf16 v[136:139], v[198:201], v[234:237], v[136:139]
	s_cmp_gt_u32 s2, 5
	s_waitcnt lgkmcnt(0)
	s_barrier
; #define LAS __attribute__((address_space(3)))
; #define MS_WLOAD(set, t) do { _Pragma("unroll") for (int r_ = 0; r_ < 4; ++r_) wr[set][r_] = __builtin_bit_cast(f32x4, __builtin_amdgcn_raw_buffer_load_b128(wrs, (int)wvo + r_ * LDW * 4, MS_CL(t) * (64 * LDW * 4), 0)); } while (0)
; #define MS_WCOMMIT(set, bufi) do { LAS unsigned char* wb_ = lds + (bufi) * MS_TILE; _Pragma("unroll") for (int i_ = 0; i_ < 4; ++i_) { \
;             u32x2 p_; p_.x = pk2(wr[set][0][i_], wr[set][1][i_]); p_.y = pk2(wr[set][2][i_], wr[set][3][i_]); \
;             *(LAS u32x2*)(wb_ + ((i_ < 2) ? lw0 : lw1) + i_ * 128) = p_; } } while (0)
; #define MS_XSLOAD(t) do { _Pragma("unroll") for (int i_ = 0; i_ < 6; ++i_) xs[i_] = __builtin_bit_cast(bf16x8, __builtin_amdgcn_raw_buffer_load_b128(xrs, (int)xso[i_], MS_CL(t) * 128, 0)); } while (0)
; #define MS_XSWRITE(bufi) do { _Pragma("unroll") for (int i_ = 0; i_ < 6; ++i_) *(LAS bf16x8*)(xw + (bufi) * MS_XBUF + i_ * 1024 + ((i_ & 1) ? (xwo ^ 64) : xwo)) = xs[i_]; } while (0)
; #define MS_STEP(I, J, t) do { MS_WCOMMIT(J, J); MS_WLOAD(J, (t) + 3); MS_COMPUTE(I); MS_XSWRITE(J); MS_XSLOAD((t) + 2); __syncthreads(); } while (0)
;     ...
;             const LAS unsigned char* xr1 = lds + MS_XOFF + wave * MS_XWAVE + tk * 128 + (((4 + q) ^ rd_g) << 4);
;             __syncthreads();
;             MS_XSLOAD(0); MS_WLOAD(0, 0); MS_WLOAD(1, 1);
;             MS_WCOMMIT(0, 0); MS_WLOAD(0, 2);
;             MS_XSWRITE(0); MS_XSLOAD(1);
;             __syncthreads();
; #pragma unroll 1
;             for (int t = 0; t < NT; t += 2) { MS_STEP(0, 1, t); MS_STEP(1, 0, t + 1); }
	v_mfma_f32_16x16x32_bf16 v[78:81], v[198:201], v[238:241], v[78:81]
	v_mfma_f32_16x16x32_bf16 v[46:49], v[198:201], v[242:245], v[46:49]
	v_mfma_f32_16x16x32_bf16 v[132:135], v[202:205], v[234:237], v[132:135]
	v_mfma_f32_16x16x32_bf16 v[74:77], v[202:205], v[238:241], v[74:77]
	v_mfma_f32_16x16x32_bf16 v[42:45], v[202:205], v[242:245], v[42:45]
	v_mfma_f32_16x16x32_bf16 v[128:131], v[206:209], v[234:237], v[128:131]
	v_mfma_f32_16x16x32_bf16 v[70:73], v[206:209], v[238:241], v[70:73]
	v_mfma_f32_16x16x32_bf16 v[38:41], v[206:209], v[242:245], v[38:41]
	v_mfma_f32_16x16x32_bf16 v[124:127], v[210:213], v[234:237], v[124:127]
	v_mfma_f32_16x16x32_bf16 v[66:69], v[210:213], v[238:241], v[66:69]
	v_mfma_f32_16x16x32_bf16 v[34:37], v[210:213], v[242:245], v[34:37]
	s_cbranch_scc0 .LBB0_1785
	s_branch .Lmoe_l_done
.Lmoe_l_b:
	s_add_i32 s2, s2, 2
	s_min_u32 s3, s2, 4
	s_lshl_b32 s33, s3, 19
	s_add_i32 s33, s33, 0x180000
	s_add_i32 s40, s85, 0x80000
	s_cmp_gt_u32 s2, 4
	s_cselect_b32 s33, s40, s33
	s_waitcnt vmcnt(10)
	v_cvt_pk_bf16_f32 v164, v2, v10
	s_waitcnt vmcnt(7)
	v_cvt_pk_bf16_f32 v165, v6, v14
	v_cvt_pk_bf16_f32 v166, v3, v11
	v_cvt_pk_bf16_f32 v167, v7, v15
	v_cvt_pk_bf16_f32 v190, v4, v12
	v_cvt_pk_bf16_f32 v191, v8, v16
	v_cvt_pk_bf16_f32 v192, v5, v13
	v_cvt_pk_bf16_f32 v193, v9, v17
	buffer_load_dwordx4 v[2:5], v160, s[8:11], s33 offen nt
	buffer_load_dwordx4 v[10:13], v90, s[8:11], s33 offen nt
	buffer_load_dwordx4 v[6:9], v178, s[8:11], s33 offen nt
	buffer_load_dwordx4 v[14:17], v179, s[8:11], s33 offen nt
	v_add_u32_e32 v194, 0x4000, v188
	v_add_u32_e32 v195, 0x4000, v180
	v_add_u32_e32 v214, v173, v174
	ds_write2_b64 v194, v[164:165], v[166:167] offset1:16
	ds_write2_b64 v195, v[190:191], v[192:193] offset0:32 offset1:48
	v_add_u32_e32 v215, v176, v174
	v_add_u32_e32 v216, v173, v175
	v_add_u32_e32 v217, v176, v175
	ds_read_b128 v[164:167], v214 offset:32768
	ds_read_b128 v[190:193], v214 offset:34816
	ds_read_b128 v[198:201], v215
	ds_read_b128 v[202:205], v215 offset:2048
	ds_read_b128 v[206:209], v215 offset:4096
	ds_read_b128 v[210:213], v215 offset:6144
	ds_read_b128 v[234:237], v216 offset:32768
	ds_read_b128 v[238:241], v216 offset:34816
	s_waitcnt lgkmcnt(5)
	v_mfma_f32_16x16x32_bf16 v[152:155], v[198:201], v[164:167], v[152:155]
	v_mfma_f32_16x16x32_bf16 v[120:123], v[198:201], v[190:193], v[120:123]
	ds_read_b128 v[198:201], v215 offset:8192
	s_waitcnt lgkmcnt(5)
	v_mfma_f32_16x16x32_bf16 v[148:151], v[202:205], v[164:167], v[148:151]
	v_mfma_f32_16x16x32_bf16 v[96:99], v[202:205], v[190:193], v[96:99]
	ds_read_b128 v[202:205], v215 offset:10240
	s_waitcnt lgkmcnt(5)
	v_mfma_f32_16x16x32_bf16 v[144:147], v[206:209], v[164:167], v[144:147]
	v_mfma_f32_16x16x32_bf16 v[86:89], v[206:209], v[190:193], v[86:89]
	ds_read_b128 v[206:209], v215 offset:12288
	s_waitcnt lgkmcnt(5)
	v_mfma_f32_16x16x32_bf16 v[140:143], v[210:213], v[164:167], v[140:143]
	v_mfma_f32_16x16x32_bf16 v[82:85], v[210:213], v[190:193], v[82:85]
	ds_read_b128 v[210:213], v215 offset:14336
	s_waitcnt lgkmcnt(3)
	v_mfma_f32_16x16x32_bf16 v[136:139], v[198:201], v[164:167], v[136:139]
	v_mfma_f32_16x16x32_bf16 v[78:81], v[198:201], v[190:193], v[78:81]
	ds_read_b128 v[198:201], v217
	s_waitcnt lgkmcnt(3)
	v_mfma_f32_16x16x32_bf16 v[132:135], v[202:205], v[164:167], v[132:135]
	v_mfma_f32_16x16x32_bf16 v[74:77], v[202:205], v[190:193], v[74:77]
	ds_read_b128 v[202:205], v217 offset:2048
	s_waitcnt lgkmcnt(3)
	v_mfma_f32_16x16x32_bf16 v[128:131], v[206:209], v[164:167], v[128:131]
	v_mfma_f32_16x16x32_bf16 v[70:73], v[206:209], v[190:193], v[70:73]
	ds_read_b128 v[206:209], v217 offset:4096
	s_waitcnt lgkmcnt(3)
	v_mfma_f32_16x16x32_bf16 v[124:127], v[210:213], v[164:167], v[124:127]
	v_mfma_f32_16x16x32_bf16 v[66:69], v[210:213], v[190:193], v[66:69]
	ds_read_b128 v[210:213], v217 offset:6144
	s_waitcnt lgkmcnt(3)
	v_mfma_f32_16x16x32_bf16 v[152:155], v[198:201], v[234:237], v[152:155]
	v_mfma_f32_16x16x32_bf16 v[120:123], v[198:201], v[238:241], v[120:123]
	ds_read_b128 v[198:201], v217 offset:8192
	s_waitcnt lgkmcnt(3)
	v_mfma_f32_16x16x32_bf16 v[148:151], v[202:205], v[234:237], v[148:151]
	v_mfma_f32_16x16x32_bf16 v[96:99], v[202:205], v[238:241], v[96:99]
	ds_read_b128 v[202:205], v217 offset:10240
	s_waitcnt lgkmcnt(3)
	v_mfma_f32_16x16x32_bf16 v[144:147], v[206:209], v[234:237], v[144:147]
	v_mfma_f32_16x16x32_bf16 v[86:89], v[206:209], v[238:241], v[86:89]
	ds_read_b128 v[206:209], v217 offset:12288
	s_waitcnt lgkmcnt(3)
	v_mfma_f32_16x16x32_bf16 v[140:143], v[210:213], v[234:237], v[140:143]
	v_mfma_f32_16x16x32_bf16 v[82:85], v[210:213], v[238:241], v[82:85]
	ds_read_b128 v[210:213], v217 offset:14336
	s_min_u32 s33, s2, 5
	s_lshl_b32 s33, s33, 7
	s_waitcnt vmcnt(7)
	ds_write_b128 v189, v[104:107] offset:38912
	s_waitcnt vmcnt(6)
	ds_write_b128 v181, v[92:95] offset:39936
	s_waitcnt vmcnt(5)
	ds_write_b128 v189, v[112:115] offset:40960
	s_waitcnt vmcnt(4)
	ds_write_b128 v181, v[116:119] offset:41984
	s_addk_i32 s33, 0x100
	s_cmp_lt_u32 s2, 6
	s_cbranch_scc1 .Lxl_nx1
	s_cmp_eq_u32 s84, 0
	s_cbranch_scc1 .Lxl_nx1
	s_mov_b32 s33, 0
	v_add_u32_e32 v252, s87, v162
	v_min_i32_e32 v253, s86, v252
	v_add_u32_e32 v253, s88, v253
	v_lshl_or_b32 v182, v253, 10, v163
	v_or_b32_e32 v253, 8, v252
	v_min_i32_e32 v253, s86, v253
	v_add_u32_e32 v253, s88, v253
	v_lshl_or_b32 v183, v253, 10, v163
	v_add_u32_e32 v253, 0x80, v252
	v_min_i32_e32 v253, s86, v253
	v_add_u32_e32 v253, s88, v253
	v_lshl_or_b32 v184, v253, 10, v163
	v_add_u32_e32 v253, 0x88, v252
	v_min_i32_e32 v253, s86, v253
	v_add_u32_e32 v253, s88, v253
	v_lshl_or_b32 v185, v253, 10, v163
	v_add_u32_e32 v253, 0x100, v252
	v_min_i32_e32 v253, s86, v253
	v_add_u32_e32 v253, s88, v253
	v_lshl_or_b32 v186, v253, 10, v163
	v_add_u32_e32 v253, 0x108, v252
	v_min_i32_e32 v253, s86, v253
	v_add_u32_e32 v253, s88, v253
	v_lshl_or_b32 v187, v253, 10, v163
.Lxl_nx1:
	s_waitcnt lgkmcnt(7)
	v_mfma_f32_16x16x32_bf16 v[136:139], v[198:201], v[234:237], v[136:139]
	buffer_load_dwordx4 v[92:95], v182, s[4:7], s33 offen
	buffer_load_dwordx4 v[100:103], v183, s[4:7], s33 offen
	buffer_load_dwordx4 v[104:107], v184, s[4:7], s33 offen
	buffer_load_dwordx4 v[108:111], v185, s[4:7], s33 offen
	s_min_u32 s33, s2, 3
	s_waitcnt lgkmcnt(0)
	v_mfma_f32_16x16x32_bf16 v[132:135], v[202:205], v[234:237], v[132:135]
	s_barrier
	s_lshl_b32 s33, s33, 19
	v_mfma_f32_16x16x32_bf16 v[128:131], v[206:209], v[234:237], v[128:131]
	s_bitset1_b32 s33, 21
	s_sub_i32 s40, s2, 4
	s_lshl_b32 s40, s40, 19
	s_add_i32 s40, s40, s85
	s_cmp_gt_u32 s2, 3
	s_cselect_b32 s33, s40, s33
	v_mfma_f32_16x16x32_bf16 v[124:127], v[210:213], v[234:237], v[124:127]
	v_cvt_pk_bf16_f32 v164, v18, v22
	v_cvt_pk_bf16_f32 v165, v26, v30
	v_cvt_pk_bf16_f32 v18, v19, v23
	v_cvt_pk_bf16_f32 v19, v27, v31
	ds_write2_b64 v188, v[164:165], v[18:19] offset1:16
	v_cvt_pk_bf16_f32 v18, v20, v24
	v_cvt_pk_bf16_f32 v19, v28, v32
	v_cvt_pk_bf16_f32 v20, v21, v25
	v_cvt_pk_bf16_f32 v21, v29, v33
	ds_write2_b64 v180, v[18:19], v[20:21] offset0:32 offset1:48
	buffer_load_dwordx4 v[18:21], v160, s[8:11], s33 offen nt
	buffer_load_dwordx4 v[22:25], v90, s[8:11], s33 offen nt
	buffer_load_dwordx4 v[26:29], v178, s[8:11], s33 offen nt
	buffer_load_dwordx4 v[30:33], v179, s[8:11], s33 offen nt
	v_mfma_f32_16x16x32_bf16 v[78:81], v[198:201], v[238:241], v[78:81]
	v_mfma_f32_16x16x32_bf16 v[74:77], v[202:205], v[238:241], v[74:77]
	v_mfma_f32_16x16x32_bf16 v[70:73], v[206:209], v[238:241], v[70:73]
	v_mfma_f32_16x16x32_bf16 v[66:69], v[210:213], v[238:241], v[66:69]
	ds_read_b128 v[164:167], v214 offset:38912
	ds_read_b128 v[190:193], v214 offset:40960
	ds_read_b128 v[198:201], v215 offset:16384
	ds_read_b128 v[202:205], v215 offset:18432
	ds_read_b128 v[206:209], v215 offset:20480
	ds_read_b128 v[210:213], v215 offset:22528
	ds_read_b128 v[234:237], v216 offset:38912
	ds_read_b128 v[238:241], v216 offset:40960
	s_waitcnt lgkmcnt(5)
	v_mfma_f32_16x16x32_bf16 v[152:155], v[198:201], v[164:167], v[152:155]
	v_mfma_f32_16x16x32_bf16 v[120:123], v[198:201], v[190:193], v[120:123]
	ds_read_b128 v[198:201], v215 offset:24576
	s_waitcnt lgkmcnt(5)
	v_mfma_f32_16x16x32_bf16 v[148:151], v[202:205], v[164:167], v[148:151]
	v_mfma_f32_16x16x32_bf16 v[96:99], v[202:205], v[190:193], v[96:99]
	ds_read_b128 v[202:205], v215 offset:26624
	s_waitcnt lgkmcnt(5)
	v_mfma_f32_16x16x32_bf16 v[144:147], v[206:209], v[164:167], v[144:147]
	v_mfma_f32_16x16x32_bf16 v[86:89], v[206:209], v[190:193], v[86:89]
	ds_read_b128 v[206:209], v215 offset:28672
	s_waitcnt lgkmcnt(5)
	v_mfma_f32_16x16x32_bf16 v[140:143], v[210:213], v[164:167], v[140:143]
	v_mfma_f32_16x16x32_bf16 v[82:85], v[210:213], v[190:193], v[82:85]
	ds_read_b128 v[210:213], v215 offset:30720
	s_waitcnt lgkmcnt(3)
	v_mfma_f32_16x16x32_bf16 v[136:139], v[198:201], v[164:167], v[136:139]
	v_mfma_f32_16x16x32_bf16 v[78:81], v[198:201], v[190:193], v[78:81]
	ds_read_b128 v[198:201], v217 offset:16384
	s_waitcnt lgkmcnt(3)
	v_mfma_f32_16x16x32_bf16 v[132:135], v[202:205], v[164:167], v[132:135]
	v_mfma_f32_16x16x32_bf16 v[74:77], v[202:205], v[190:193], v[74:77]
	ds_read_b128 v[202:205], v217 offset:18432
	s_waitcnt lgkmcnt(3)
	v_mfma_f32_16x16x32_bf16 v[128:131], v[206:209], v[164:167], v[128:131]
	v_mfma_f32_16x16x32_bf16 v[70:73], v[206:209], v[190:193], v[70:73]
	ds_read_b128 v[206:209], v217 offset:20480
	s_waitcnt lgkmcnt(3)
	v_mfma_f32_16x16x32_bf16 v[124:127], v[210:213], v[164:167], v[124:127]
	v_mfma_f32_16x16x32_bf16 v[66:69], v[210:213], v[190:193], v[66:69]
	ds_read_b128 v[210:213], v217 offset:22528
	s_waitcnt lgkmcnt(3)
	v_mfma_f32_16x16x32_bf16 v[152:155], v[198:201], v[234:237], v[152:155]
	v_mfma_f32_16x16x32_bf16 v[120:123], v[198:201], v[238:241], v[120:123]
	ds_read_b128 v[198:201], v217 offset:24576
	s_waitcnt lgkmcnt(3)
	v_mfma_f32_16x16x32_bf16 v[148:151], v[202:205], v[234:237], v[148:151]
	v_mfma_f32_16x16x32_bf16 v[96:99], v[202:205], v[238:241], v[96:99]
	ds_read_b128 v[202:205], v217 offset:26624
	s_waitcnt lgkmcnt(3)
	v_mfma_f32_16x16x32_bf16 v[144:147], v[206:209], v[234:237], v[144:147]
	v_mfma_f32_16x16x32_bf16 v[86:89], v[206:209], v[238:241], v[86:89]
	ds_read_b128 v[206:209], v217 offset:28672
	s_waitcnt lgkmcnt(3)
	v_mfma_f32_16x16x32_bf16 v[140:143], v[210:213], v[234:237], v[140:143]
	v_mfma_f32_16x16x32_bf16 v[82:85], v[210:213], v[238:241], v[82:85]
	ds_read_b128 v[210:213], v217 offset:30720
	s_lshl_b32 s3, s3, 7
	s_waitcnt vmcnt(7)
	ds_write_b128 v189, v[92:95] offset:32768
	s_waitcnt vmcnt(6)
	ds_write_b128 v181, v[100:103] offset:33792
	s_waitcnt vmcnt(5)
	ds_write_b128 v189, v[104:107] offset:34816
	s_waitcnt vmcnt(4)
	ds_write_b128 v181, v[108:111] offset:35840
	s_addk_i32 s3, 0x180
	s_cmp_eq_u32 s2, 6
	s_cselect_b32 s40, s84, 0
	s_cmp_lg_u32 s40, 0
	s_cselect_b32 s3, 0x80, s3
	buffer_load_dwordx4 v[104:107], v182, s[4:7], s3 offen
	buffer_load_dwordx4 v[92:95], v183, s[4:7], s3 offen
	buffer_load_dwordx4 v[112:115], v184, s[4:7], s3 offen
	buffer_load_dwordx4 v[116:119], v185, s[4:7], s3 offen
	s_waitcnt lgkmcnt(7)
	v_mfma_f32_16x16x32_bf16 v[136:139], v[198:201], v[234:237], v[136:139]
	s_cmp_gt_u32 s2, 5
	s_waitcnt lgkmcnt(0)
	s_barrier
	v_mfma_f32_16x16x32_bf16 v[78:81], v[198:201], v[238:241], v[78:81]
	v_mfma_f32_16x16x32_bf16 v[132:135], v[202:205], v[234:237], v[132:135]
	v_mfma_f32_16x16x32_bf16 v[74:77], v[202:205], v[238:241], v[74:77]
	v_mfma_f32_16x16x32_bf16 v[128:131], v[206:209], v[234:237], v[128:131]
	v_mfma_f32_16x16x32_bf16 v[70:73], v[206:209], v[238:241], v[70:73]
	v_mfma_f32_16x16x32_bf16 v[124:127], v[210:213], v[234:237], v[124:127]
	v_mfma_f32_16x16x32_bf16 v[66:69], v[210:213], v[238:241], v[66:69]
	s_cbranch_scc0 .Lmoe_l_b
